# fp8 K-loop: removed compiler mid-segment lgkmcnt(0) between B and A fragment reads (G3,G4)
# speedup vs baseline: 1.0085x; 1.0003x over previous
.LBB0_1398:
	v_add_u32_e32 v0, s41, v217
	v_add_u32_e32 v12, s44, v217
	ds_read_b128 v[16:19], v0
	ds_read_b128 v[20:23], v0 offset:1024
	ds_read_b128 v[24:27], v0 offset:2048
	ds_read_b128 v[28:31], v0 offset:3072
	ds_read_b128 v[0:3], v12
	ds_read_b128 v[4:7], v12 offset:1024
	ds_read_b128 v[8:11], v12 offset:2048
	ds_read_b128 v[12:15], v12 offset:3072
	s_cmp_eq_u32 s67, 4
	s_cselect_b64 s[0:1], -1, 0
	v_mov_b32_e32 v64, v214
	ds_read_b128 v[56:59], v218
	ds_read_b128 v[60:63], v218 offset:1024
	ds_read_b128 v[48:51], v218 offset:2048
	ds_read_b128 v[52:55], v218 offset:3072
	ds_read_b128 v[40:43], v218 offset:4096
	ds_read_b128 v[44:47], v218 offset:5120
	ds_read_b128 v[32:35], v218 offset:6144
	ds_read_b128 v[36:39], v218 offset:7168
	s_add_i32 m0, s19, 0xc000
	s_and_b64 s[2:3], s[20:21], s[0:1]
	global_load_lds_dwordx4 v64, s[26:27]
	v_mov_b32_e32 v64, v216
	s_add_i32 m0, s19, 0xe000
	s_andn2_b64 vcc, exec, s[2:3]
	global_load_lds_dwordx4 v64, s[26:27]
	s_cbranch_vccnz .LBB0_1400
	s_mov_b32 s2, s86
	v_mbcnt_lo_u32_b32 v64, -1, 0
	v_mbcnt_hi_u32_b32 v64, -1, v64
	s_nop 0
	v_lshl_add_u32 v64, s2, 6, v64
	s_nop 0
	v_ashrrev_i32_e32 v67, 31, v64
	v_lshrrev_b32_e32 v67, 26, v67
	v_lshlrev_b32_e32 v215, 4, v64
	v_lshlrev_b32_e32 v66, 2, v64
	v_add_u32_e32 v67, v64, v67
	v_bfe_i32 v64, v64, 27, 1
	v_lshrrev_b32_e32 v64, 22, v64
	v_add_u32_e32 v64, v215, v64
	v_and_b32_e32 v64, 0xfffffc00, v64
	v_sub_u32_e32 v64, v215, v64
	v_lshrrev_b32_e32 v213, 4, v64
	v_bitop3_b32 v213, v213, v64, 32 bitop3:0x6c
	v_ashrrev_i32_e32 v64, 31, v64
	v_lshrrev_b32_e32 v64, 26, v64
	v_add_u32_e32 v64, v213, v64
	v_and_b32_e32 v66, 0xfc, v66
	v_and_b32_e32 v64, 0xc0, v64
	v_lshrrev_b32_e32 v67, 1, v67
	v_sub_u32_e32 v64, v213, v64
	v_add_u32_e32 v213, s40, v66
	v_and_b32_e32 v214, 32, v67
	ds_read2st64_b32 v[66:67], v213 offset1:1
	ds_read2st64_b32 v[220:221], v213 offset0:2 offset1:3
	v_ashrrev_i16_sdwa v64, v201, sext(v64) dst_sel:DWORD dst_unused:UNUSED_PAD src0_sel:DWORD src1_sel:BYTE_0
	v_bfe_i32 v64, v64, 0, 16
	v_add_lshl_u32 v64, v214, v64, 1
	s_waitcnt lgkmcnt(0)
	v_lshl_add_u32 v213, v66, 10, v64
	v_lshl_add_u32 v214, v220, 10, v64
	v_add_u32_e32 v64, 0x2000, v215
	v_ashrrev_i32_e32 v66, 31, v64
	v_lshrrev_b32_e32 v66, 22, v66
	v_add_u32_e32 v66, v64, v66
	v_ashrrev_i32_e32 v66, 10, v66
	v_mul_i32_i24_e32 v215, 0x400, v66
	v_sub_u32_e32 v64, v64, v215
	v_lshrrev_b32_e32 v215, 4, v64
	v_bitop3_b32 v215, v215, v64, 32 bitop3:0x6c
	v_ashrrev_i32_e32 v64, 31, v64
	v_lshrrev_b32_e32 v64, 26, v64
	v_add_u32_e32 v64, v215, v64
	v_and_b32_e32 v64, 0xc0, v64
	v_sub_u32_e32 v64, v215, v64
	v_lshlrev_b32_e32 v66, 5, v66
	v_ashrrev_i16_sdwa v64, v201, sext(v64) dst_sel:DWORD dst_unused:UNUSED_PAD src0_sel:DWORD src1_sel:BYTE_0
	v_and_b32_e32 v66, 32, v66
	v_bfe_i32 v64, v64, 0, 16
	v_add_lshl_u32 v64, v66, v64, 1
	v_lshl_add_u32 v215, v67, 10, v64
	v_lshl_add_u32 v216, v221, 10, v64

.LBB0_1404:
	s_barrier
	v_add_u32_e32 v0, s52, v217
	v_add_u32_e32 v12, s57, v217
	ds_read_b128 v[16:19], v0
	ds_read_b128 v[20:23], v0 offset:1024
	ds_read_b128 v[24:27], v0 offset:2048
	ds_read_b128 v[28:31], v0 offset:3072
	ds_read_b128 v[0:3], v12
	ds_read_b128 v[4:7], v12 offset:1024
	ds_read_b128 v[8:11], v12 offset:2048
	ds_read_b128 v[12:15], v12 offset:3072
	v_mov_b32_e32 v64, v214
	s_mov_b32 m0, s48
	ds_read_b128 v[56:59], v218 offset:32768
	ds_read_b128 v[60:63], v218 offset:33792
	ds_read_b128 v[48:51], v218 offset:34816
	ds_read_b128 v[52:55], v218 offset:35840
	ds_read_b128 v[40:43], v218 offset:36864
	ds_read_b128 v[44:47], v218 offset:37888
	ds_read_b128 v[32:35], v218 offset:38912
	ds_read_b128 v[36:39], v218 offset:39936
	s_and_b64 vcc, exec, s[2:3]
	global_load_lds_dwordx4 v64, s[28:29]
	v_mov_b32_e32 v64, v216
	s_mov_b32 m0, s49
	s_nop 0
	global_load_lds_dwordx4 v64, s[28:29]
	s_waitcnt vmcnt(8)
	s_waitcnt lgkmcnt(0)
	s_barrier
	s_cbranch_vccnz .LBB0_1406
	s_setprio 1
	s_waitcnt lgkmcnt(0)
	v_mfma_f32_16x16x128_f8f6f4 v[192:195], v[16:23], v[56:63], v[192:195]
	v_mfma_f32_16x16x128_f8f6f4 v[184:187], v[24:31], v[56:63], v[184:187]
	v_mfma_f32_16x16x128_f8f6f4 v[176:179], v[16:23], v[48:55], v[176:179]
	v_mfma_f32_16x16x128_f8f6f4 v[168:171], v[24:31], v[48:55], v[168:171]
	v_mfma_f32_16x16x128_f8f6f4 v[160:163], v[16:23], v[40:47], v[160:163]
	v_mfma_f32_16x16x128_f8f6f4 v[152:155], v[24:31], v[40:47], v[152:155]
	v_mfma_f32_16x16x128_f8f6f4 v[144:147], v[16:23], v[32:39], v[144:147]
	v_mfma_f32_16x16x128_f8f6f4 v[136:139], v[24:31], v[32:39], v[136:139]
	s_setprio 0
	s_setprio 1
	v_mfma_f32_16x16x128_f8f6f4 v[188:191], v[0:7], v[56:63], v[188:191]
	v_mfma_f32_16x16x128_f8f6f4 v[180:183], v[8:15], v[56:63], v[180:183]
	v_mfma_f32_16x16x128_f8f6f4 v[172:175], v[0:7], v[48:55], v[172:175]
	v_mfma_f32_16x16x128_f8f6f4 v[164:167], v[8:15], v[48:55], v[164:167]
	v_mfma_f32_16x16x128_f8f6f4 v[156:159], v[0:7], v[40:47], v[156:159]
	v_mfma_f32_16x16x128_f8f6f4 v[148:151], v[8:15], v[40:47], v[148:151]
	v_mfma_f32_16x16x128_f8f6f4 v[140:143], v[0:7], v[32:39], v[140:143]
	v_mfma_f32_16x16x128_f8f6f4 v[132:135], v[8:15], v[32:39], v[132:135]
	s_setprio 0

.LBB0_1476:
	v_add_u32_e32 v0, s23, v215
	v_add_u32_e32 v12, s43, v215
	ds_read_b128 v[16:19], v0
	ds_read_b128 v[20:23], v0 offset:1024
	ds_read_b128 v[24:27], v0 offset:2048
	ds_read_b128 v[28:31], v0 offset:3072
	ds_read_b128 v[0:3], v12
	ds_read_b128 v[4:7], v12 offset:1024
	ds_read_b128 v[8:11], v12 offset:2048
	ds_read_b128 v[12:15], v12 offset:3072
	v_mov_b32_e32 v64, v212
	ds_read_b128 v[56:59], v216
	ds_read_b128 v[60:63], v216 offset:1024
	ds_read_b128 v[48:51], v216 offset:2048
	ds_read_b128 v[52:55], v216 offset:3072
	ds_read_b128 v[40:43], v216 offset:4096
	ds_read_b128 v[44:47], v216 offset:5120
	ds_read_b128 v[32:35], v216 offset:6144
	ds_read_b128 v[36:39], v216 offset:7168
	s_add_i32 m0, s46, 0xc000
	s_andn2_b64 vcc, exec, s[28:29]
	global_load_lds_dwordx4 v64, s[30:31]
	v_mov_b32_e32 v64, v214
	s_add_i32 m0, s46, 0xe000
	s_nop 0
	global_load_lds_dwordx4 v64, s[30:31]
	s_waitcnt vmcnt(8)
	s_waitcnt lgkmcnt(0)
	v_cndmask_b32_e64 v64, 0, 1, s[28:29]
	v_cmp_ne_u32_e64 s[2:3], 1, v64
	s_barrier
	s_cbranch_vccnz .LBB0_1478
	s_setprio 1
	s_waitcnt lgkmcnt(0)
	v_mfma_f32_16x16x128_f8f6f4 v[192:195], v[16:23], v[56:63], v[192:195]
	v_mfma_f32_16x16x128_f8f6f4 v[188:191], v[24:31], v[56:63], v[188:191]
	v_mfma_f32_16x16x128_f8f6f4 v[176:179], v[16:23], v[48:55], v[176:179]
	v_mfma_f32_16x16x128_f8f6f4 v[172:175], v[24:31], v[48:55], v[172:175]
	v_mfma_f32_16x16x128_f8f6f4 v[160:163], v[16:23], v[40:47], v[160:163]
	v_mfma_f32_16x16x128_f8f6f4 v[156:159], v[24:31], v[40:47], v[156:159]
	v_mfma_f32_16x16x128_f8f6f4 v[144:147], v[16:23], v[32:39], v[144:147]
	v_mfma_f32_16x16x128_f8f6f4 v[140:143], v[24:31], v[32:39], v[140:143]
	s_setprio 0
	s_setprio 1
	v_mfma_f32_16x16x128_f8f6f4 v[184:187], v[0:7], v[56:63], v[184:187]
	v_mfma_f32_16x16x128_f8f6f4 v[180:183], v[8:15], v[56:63], v[180:183]
	v_mfma_f32_16x16x128_f8f6f4 v[168:171], v[0:7], v[48:55], v[168:171]
	v_mfma_f32_16x16x128_f8f6f4 v[164:167], v[8:15], v[48:55], v[164:167]
	v_mfma_f32_16x16x128_f8f6f4 v[152:155], v[0:7], v[40:47], v[152:155]
	v_mfma_f32_16x16x128_f8f6f4 v[148:151], v[8:15], v[40:47], v[148:151]
	v_mfma_f32_16x16x128_f8f6f4 v[136:139], v[0:7], v[32:39], v[136:139]
	v_mfma_f32_16x16x128_f8f6f4 v[132:135], v[8:15], v[32:39], v[132:135]
	s_setprio 0

.LBB0_1480:
	s_barrier
	v_add_u32_e32 v0, s52, v215
	v_add_u32_e32 v12, s57, v215
	ds_read_b128 v[16:19], v0
	ds_read_b128 v[20:23], v0 offset:1024
	ds_read_b128 v[24:27], v0 offset:2048
	ds_read_b128 v[28:31], v0 offset:3072
	ds_read_b128 v[0:3], v12
	ds_read_b128 v[4:7], v12 offset:1024
	ds_read_b128 v[8:11], v12 offset:2048
	ds_read_b128 v[12:15], v12 offset:3072
	s_add_u32 s66, s34, 0x40000
	v_mov_b32_e32 v64, v212
	s_mov_b32 m0, s48
	ds_read_b128 v[56:59], v216 offset:32768
	ds_read_b128 v[60:63], v216 offset:33792
	ds_read_b128 v[48:51], v216 offset:34816
	ds_read_b128 v[52:55], v216 offset:35840
	ds_read_b128 v[40:43], v216 offset:36864
	ds_read_b128 v[44:47], v216 offset:37888
	ds_read_b128 v[32:35], v216 offset:38912
	ds_read_b128 v[36:39], v216 offset:39936
	s_addc_u32 s67, s35, 0
	s_and_b64 vcc, exec, s[2:3]
	global_load_lds_dwordx4 v64, s[66:67]
	v_mov_b32_e32 v64, v214
	s_mov_b32 m0, s49
	s_nop 0
	global_load_lds_dwordx4 v64, s[66:67]
	s_waitcnt vmcnt(8)
	s_waitcnt lgkmcnt(0)
	s_barrier
	s_cbranch_vccnz .LBB0_1482
	s_setprio 1
	s_waitcnt lgkmcnt(0)
	v_mfma_f32_16x16x128_f8f6f4 v[192:195], v[16:23], v[56:63], v[192:195]
	v_mfma_f32_16x16x128_f8f6f4 v[188:191], v[24:31], v[56:63], v[188:191]
	v_mfma_f32_16x16x128_f8f6f4 v[176:179], v[16:23], v[48:55], v[176:179]
	v_mfma_f32_16x16x128_f8f6f4 v[172:175], v[24:31], v[48:55], v[172:175]
	v_mfma_f32_16x16x128_f8f6f4 v[160:163], v[16:23], v[40:47], v[160:163]
	v_mfma_f32_16x16x128_f8f6f4 v[156:159], v[24:31], v[40:47], v[156:159]
	v_mfma_f32_16x16x128_f8f6f4 v[144:147], v[16:23], v[32:39], v[144:147]
	v_mfma_f32_16x16x128_f8f6f4 v[140:143], v[24:31], v[32:39], v[140:143]
	s_setprio 0
	s_setprio 1
	v_mfma_f32_16x16x128_f8f6f4 v[184:187], v[0:7], v[56:63], v[184:187]
	v_mfma_f32_16x16x128_f8f6f4 v[180:183], v[8:15], v[56:63], v[180:183]
	v_mfma_f32_16x16x128_f8f6f4 v[168:171], v[0:7], v[48:55], v[168:171]
	v_mfma_f32_16x16x128_f8f6f4 v[164:167], v[8:15], v[48:55], v[164:167]
	v_mfma_f32_16x16x128_f8f6f4 v[152:155], v[0:7], v[40:47], v[152:155]
	v_mfma_f32_16x16x128_f8f6f4 v[148:151], v[8:15], v[40:47], v[148:151]
	v_mfma_f32_16x16x128_f8f6f4 v[136:139], v[0:7], v[32:39], v[136:139]
	v_mfma_f32_16x16x128_f8f6f4 v[132:135], v[8:15], v[32:39], v[132:135]
	s_setprio 0
